# speedup vs baseline: 1.0799x; 1.0130x over previous
_Z7k_finalPKfPKiPf:
	s_load_dwordx4 s[4:7], s[0:1], 0x0
	s_load_dwordx2 s[8:9], s[0:1], 0x10
	s_mul_hi_u32 s3, s2, 0xaaaaaaab
	v_lshrrev_b32_e32 v1, 6, v0
	v_and_b32_e32 v2, 63, v0
	s_lshr_b32 s10, s3, 1
	s_mul_i32 s3, s10, 3
	s_sub_i32 s11, s2, s3
	s_mul_i32 s12, s10, 0xc000
	s_lshl_b32 s13, s11, 8
	s_add_u32 s12, s12, s13
	v_mul_u32_u24_e32 v3, 0x3000, v1
	v_lshl_add_u32 v3, v2, 2, v3
	v_add_u32_e32 v3, s12, v3
	v_add_u32_e32 v4, 0x1200, v3
	v_add_u32_e32 v5, 0x2400, v3
	v_lshlrev_b32_e32 v6, 2, v0
	v_lshlrev_b32_e32 v8, 2, v2
	v_mov_b32_e32 v9, 0
	v_readfirstlane_b32 s14, v1
	v_lshl_or_b32 v29, v1, 8, v8
	s_waitcnt lgkmcnt(0)
	global_load_dword v7, v6, s[6:7]
	global_load_dword v10, v3, s[4:5]
	global_load_dword v18, v3, s[4:5] offset:768
	global_load_dword v11, v3, s[4:5] offset:1536
	global_load_dword v19, v3, s[4:5] offset:2304
	global_load_dword v12, v3, s[4:5] offset:3072
	global_load_dword v20, v3, s[4:5] offset:3840
	global_load_dword v13, v4, s[4:5]
	global_load_dword v21, v4, s[4:5] offset:768
	global_load_dword v14, v4, s[4:5] offset:1536
	global_load_dword v22, v4, s[4:5] offset:2304
	global_load_dword v15, v4, s[4:5] offset:3072
	global_load_dword v23, v4, s[4:5] offset:3840
	global_load_dword v16, v5, s[4:5]
	global_load_dword v24, v5, s[4:5] offset:768
	global_load_dword v17, v5, s[4:5] offset:1536
	global_load_dword v25, v5, s[4:5] offset:2304
	s_lshl_b32 s19, s14, 3
	v_mov_b32_e32 v28, s19
	s_waitcnt vmcnt(16)
	s_nop 0
	v_add_u32_dpp v7, v7, v7 quad_perm:[1,0,3,2] row_mask:0xf bank_mask:0xf
	s_nop 1
	v_add_u32_dpp v7, v7, v7 quad_perm:[2,3,0,1] row_mask:0xf bank_mask:0xf
	s_nop 1
	v_add_u32_dpp v7, v7, v7 row_half_mirror row_mask:0xf bank_mask:0xf
	s_nop 1
	v_add_u32_dpp v7, v7, v7 row_mirror row_mask:0xf bank_mask:0xf
	s_nop 1
	v_readlane_b32 s15, v7, 0
	v_readlane_b32 s16, v7, 16
	v_readlane_b32 s17, v7, 32
	v_readlane_b32 s18, v7, 48
	s_add_u32 s15, s15, s16
	s_add_u32 s17, s17, s18
	v_mov_b32_e32 v26, s15
	v_mov_b32_e32 v27, s17
	s_mov_b64 exec, 1
	ds_write_b64 v28, v[26:27] offset:2048
	s_mov_b64 exec, -1
	s_waitcnt vmcnt(0)
	v_add_f32_e32 v10, v10, v11
	v_add_f32_e32 v12, v12, v13
	v_add_f32_e32 v14, v14, v15
	v_add_f32_e32 v16, v16, v17
	v_add_f32_e32 v18, v18, v19
	v_add_f32_e32 v20, v20, v21
	v_add_f32_e32 v22, v22, v23
	v_add_f32_e32 v24, v24, v25
	v_add_f32_e32 v10, v10, v12
	v_add_f32_e32 v14, v14, v16
	v_add_f32_e32 v18, v18, v20
	v_add_f32_e32 v22, v22, v24
	v_add_f32_e32 v10, v10, v14
	v_add_f32_e32 v18, v18, v22
	ds_write2st64_b32 v29, v10, v18 offset1:4
	s_waitcnt lgkmcnt(0)
	s_barrier
	s_cmp_lg_u32 s14, 0
	s_cbranch_scc1 .Lf_end
	ds_read2st64_b32 v[10:11], v8 offset1:1
	ds_read2st64_b32 v[12:13], v8 offset0:2 offset1:3
	ds_read2st64_b32 v[14:15], v8 offset0:4 offset1:5
	ds_read2st64_b32 v[16:17], v8 offset0:6 offset1:7
	s_mov_b64 exec, 0xff
	ds_read_b32 v20, v8 offset:2048
	s_mov_b64 exec, -1
	s_waitcnt lgkmcnt(1)
	v_add_f32_e32 v10, v10, v11
	v_add_f32_e32 v12, v12, v13
	v_add_f32_e32 v14, v14, v15
	v_add_f32_e32 v16, v16, v17
	v_add_f32_e32 v30, v10, v12
	v_add_f32_e32 v31, v14, v16
	s_waitcnt lgkmcnt(0)
	v_cmp_lt_i32_e64 s[20:21], 9, v20
	v_add_f32_dpp v32, v30, v30 quad_perm:[1,0,3,2] row_mask:0xf bank_mask:0xf
	v_add_f32_dpp v33, v31, v31 quad_perm:[1,0,3,2] row_mask:0xf bank_mask:0xf
	s_and_b32 s20, s20, 0xff
	s_bcnt1_i32_b32 s22, s20
	s_nop 0
	v_add_f32_dpp v32, v32, v32 quad_perm:[2,3,0,1] row_mask:0xf bank_mask:0xf
	v_add_f32_dpp v33, v33, v33 quad_perm:[2,3,0,1] row_mask:0xf bank_mask:0xf
	s_max_u32 s22, s22, 1
	s_mulk_i32 s22, 0xc0
	s_nop 0
	v_add_f32_dpp v32, v32, v32 row_half_mirror row_mask:0xf bank_mask:0xf
	v_add_f32_dpp v33, v33, v33 row_half_mirror row_mask:0xf bank_mask:0xf
	s_bitcmp1_b32 s20, s10
	s_cselect_b32 s23, 1.0, 0
	s_nop 0
	v_add_f32_dpp v32, v32, v32 row_mirror row_mask:0xf bank_mask:0xf
	v_add_f32_dpp v33, v33, v33 row_mirror row_mask:0xf bank_mask:0xf
	v_cvt_f32_u32_e32 v35, s22
	s_nop 0
	v_readlane_b32 s12, v32, 0
	v_readlane_b32 s13, v32, 16
	v_readlane_b32 s15, v32, 32
	v_readlane_b32 s16, v32, 48
	v_readlane_b32 s17, v33, 0
	v_readlane_b32 s18, v33, 16
	v_readlane_b32 s19, v33, 32
	v_readlane_b32 s24, v33, 48
	v_mov_b32_e32 v3, s13
	v_mov_b32_e32 v4, s16
	v_mov_b32_e32 v5, s18
	v_mov_b32_e32 v6, s24
	v_add_f32_e32 v3, s12, v3
	v_add_f32_e32 v4, s15, v4
	v_add_f32_e32 v5, s17, v5
	v_add_f32_e32 v6, s19, v6
	v_add_f32_e32 v3, v3, v4
	v_add_f32_e32 v5, v5, v6
	v_add_f32_e32 v3, 0x322bcc77, v3
	v_add_f32_e32 v5, 0x322bcc77, v5
	v_div_scale_f32 v10, s[12:13], v3, v3, v30
	v_div_scale_f32 v11, s[12:13], v5, v5, v31
	v_rcp_f32_e32 v12, v10
	v_rcp_f32_e32 v13, v11
	v_div_scale_f32 v14, vcc, v30, v3, v30
	v_div_scale_f32 v15, s[16:17], v31, v5, v31
	v_fma_f32 v16, -v10, v12, 1.0
	v_fma_f32 v17, -v11, v13, 1.0
	v_fmac_f32_e32 v12, v16, v12
	v_fmac_f32_e32 v13, v17, v13
	v_mul_f32_e32 v16, v14, v12
	v_mul_f32_e32 v17, v15, v13
	v_fma_f32 v18, -v10, v16, v14
	v_fma_f32 v19, -v11, v17, v15
	v_fmac_f32_e32 v16, v18, v12
	v_fmac_f32_e32 v17, v19, v13
	v_fma_f32 v10, -v10, v16, v14
	v_fma_f32 v11, -v11, v17, v15
	v_div_fmas_f32 v10, v10, v12, v16
	s_mov_b64 vcc, s[16:17]
	s_nop 3
	v_div_fmas_f32 v11, v11, v13, v17
	v_div_fixup_f32 v10, v10, v3, v30
	v_div_fixup_f32 v11, v11, v5, v31
	v_sub_f32_e32 v10, v10, v11
	v_and_b32_e32 v11, 0x7fffffff, v10
	s_nop 1
	v_add_f32_dpp v10, v11, |v10| quad_perm:[1,0,3,2] row_mask:0xf bank_mask:0xf
	s_nop 1
	v_add_f32_dpp v10, v10, v10 quad_perm:[2,3,0,1] row_mask:0xf bank_mask:0xf
	s_nop 1
	v_add_f32_dpp v10, v10, v10 row_half_mirror row_mask:0xf bank_mask:0xf
	s_nop 1
	v_add_f32_dpp v10, v10, v10 row_mirror row_mask:0xf bank_mask:0xf
	s_nop 1
	v_readlane_b32 s12, v10, 0
	v_readlane_b32 s13, v10, 16
	v_readlane_b32 s15, v10, 32
	v_readlane_b32 s16, v10, 48
	s_mov_b64 exec, 1
	v_mov_b32_e32 v3, s13
	v_mov_b32_e32 v4, s16
	v_add_f32_e32 v3, s12, v3
	v_add_f32_e32 v4, s15, v4
	v_add_f32_e32 v3, v3, v4
	v_mul_f32_e32 v3, s23, v3
	v_div_scale_f32 v4, s[12:13], v35, v35, v3
	v_rcp_f32_e32 v5, v4
	v_div_scale_f32 v6, vcc, v3, v35, v3
	v_fma_f32 v7, -v4, v5, 1.0
	v_fmac_f32_e32 v5, v7, v5
	v_mul_f32_e32 v7, v6, v5
	v_fma_f32 v10, -v4, v7, v6
	v_fmac_f32_e32 v7, v10, v5
	v_fma_f32 v4, -v4, v7, v6
	v_div_fmas_f32 v4, v4, v5, v7
	v_div_fixup_f32 v3, v4, v35, v3
	global_atomic_add_f32 v9, v3, s[8:9]
